# v33 + SB unit header: dropped the vmcnt(0) that waited for the previous unit's output stores before issuing q loads and tile DMAs
# speedup vs baseline: 1.0103x; 1.0103x over previous
; #define GAS __attribute__((address_space(1)))
; #define LAS __attribute__((address_space(3)))
; #define GAS __attribute__((address_space(1)))
; #define SB_ISSUE(j) do { int kt_ = kt_hi - (j); kt_ = kt_ < 0 ? 0 : kt_; LAS unsigned char* sl_ = lds + ((j) % NS) * 16384 + wid * 1024; \
;         dma16(ksrc + (size_t)kt_ * 64 * 1536, sl_); dma16(vsrc + (size_t)kt_ * 64 * 1536, sl_ + 8192); } while (0)
; __device__ __forceinline__ void sb_unit(LAS unsigned char* lds, int tid, const bf16_t* QKV, bf16_t* OA, float* OSS, int b, int h, int qb) {
;     asm volatile("" : "+v"(tid));
;     const int lane = tid & 63, r32 = lane & 31, hi = lane >> 5, wid = __builtin_amdgcn_readfirstlane(tid >> 6);
;     const size_t rowb = (size_t)b * SEQ; const int q0 = qb * 256;
;     const bf16_t* Qw = QKV + (rowb + q0 + wid * 32) * 1536 + h * 64;
;     const bf16_t* Kh = QKV + rowb * 1536 + 512 + h * 64; const bf16_t* Vh = Kh + 512;
;     const int kt_hi = (q0 >> 6) + 3, NT = kt_hi + 1, jd = 3 - (wid >> 1);
;     const bf16_t* ksrc = Kh + (size_t)lane * 1536 + wid * 8;
;     const bf16_t* vsrc = Vh + (size_t)(16 * (wid & 3) + (lane >> 2)) * 1536 + (wid >> 2) * 32 + (lane & 3) * 8;
;     ...
;     bf16x8 qr[4];
; #pragma unroll
;     for (int d0 = 0; d0 < 4; ++d0) qr[d0] = *(const GAS bf16x8*)(Qw + (size_t)r32 * 1536 + d0 * 16 + hi * 8);
; #pragma unroll
;     for (int j = 0; j < PF; ++j) SB_ISSUE(j);
;     asm volatile("" : "+v"(qr[0]), "+v"(qr[1]), "+v"(qr[2]), "+v"(qr[3]));
;     f32x16 o0 = {}, o1 = {}; float carry = 1.f; bool mydone = false;
;     const int q = q0 + wid * 32 + r32;
;     volatile LAS unsigned* flags = (volatile LAS unsigned*)(lds + FLAG_OFF);
;     const int vpo = ((lane >> 4) & 1) * 32 + (lane & 3) * 8 + (4 * hi + ((lane & 15) >> 2)) * 64;
.LBB0_876:
	v_mov_b32_e32 v8, v188
	s_ashr_i32 s8, s79, 7
	s_and_b32 s2, s78, 15
	v_readfirstlane_b32 s13, v8
	s_and_b32 s12, s79, 15
	s_ashr_i32 s14, s13, 6
	s_ashr_i32 s9, s8, 31
	s_lshl_b32 s95, s2, 2
	s_lshl_b64 s[90:91], s[8:9], 12
	s_lshl_b32 s2, s12, 8
	s_lshl_b32 s3, s14, 5
	s_bfe_u32 s94, s79, 0x30004
	v_writelane_b32 v255, s2, 42
	s_or_b32 s2, s90, s2
	s_ashr_i32 s6, s3, 31
	s_add_u32 s2, s2, s3
	s_addc_u32 s6, s91, s6
	s_mulk_i32 s6, 0xc00
	s_mul_hi_u32 s7, s2, 0xc00
	s_add_i32 s7, s7, s6
	s_mulk_i32 s2, 0xc00
	v_readlane_b32 s10, v255, 40
	s_add_u32 s2, s10, s2
	v_readlane_b32 s11, v255, 41
	v_and_b32_e32 v115, 31, v8
	s_addc_u32 s7, s11, s7
	s_lshl_b32 s6, s94, 6
	s_lshl_b32 s9, s94, 7
	v_writelane_b32 v255, s6, 43
	s_add_u32 s6, s2, s9
	v_mul_u32_u24_e32 v0, 0x600, v115
	v_bfe_u32 v9, v8, 5, 1
	s_addc_u32 s7, s7, 0
	v_lshlrev_b32_e32 v0, 1, v0
	v_lshl_add_u64 v[2:3], s[6:7], 0, v[0:1]
	v_lshlrev_b32_e32 v0, 4, v9
	v_lshl_add_u64 v[2:3], v[2:3], 0, v[0:1]
	global_load_dwordx4 v[66:69], v[2:3], off offset:96
	global_load_dwordx4 v[70:73], v[2:3], off offset:64
	global_load_dwordx4 v[74:77], v[2:3], off offset:32
	global_load_dwordx4 v[78:81], v[2:3], off
	s_mul_i32 s7, s8, 0xc00000
	s_mul_hi_i32 s6, s8, 0xc00000
	s_add_u32 s7, s10, s7
	s_addc_u32 s8, s11, s6
	s_add_u32 s6, s7, s9
	s_waitcnt lgkmcnt(8)
	v_and_b32_e32 v120, 63, v8
	s_addc_u32 s7, s8, 0
	s_lshl_b32 s10, s14, 4
	v_bfe_u32 v2, v8, 2, 4
	v_mul_u32_u24_e32 v0, 0x600, v120
	v_and_or_b32 v2, s10, 48, v2
	s_lshl_b32 s82, s12, 2
	s_lshl_b32 s8, s14, 3
	v_mul_u32_u24_e32 v4, 0x600, v2
	s_ashr_i32 s10, s13, 3
	v_lshlrev_b32_e32 v2, 3, v8
	v_lshlrev_b32_e32 v0, 1, v0
	s_ashr_i32 s9, s8, 31
	s_andn2_b32 s10, s10, 31
	v_and_b32_e32 v10, 24, v2
	s_or_b32 s15, s82, 3
	v_lshl_add_u64 v[2:3], s[6:7], 0, v[0:1]
	v_lshlrev_b32_e32 v0, 1, v4
	s_ashr_i32 s11, s10, 31
	v_lshl_add_u64 v[116:117], s[8:9], 1, v[2:3]
	v_lshl_add_u64 v[4:5], s[6:7], 0, v[0:1]
	s_mul_i32 s88, s15, 0x30000
	v_lshl_add_u64 v[4:5], s[10:11], 1, v[4:5]
	v_lshlrev_b32_e32 v0, 1, v10
	s_lshl_b32 s6, s14, 10
	v_lshl_add_u64 v[6:7], v[116:117], 0, s[88:89]
	v_lshl_add_u64 v[118:119], v[4:5], 0, v[0:1]
	s_add_i32 s33, s6, 0
	v_lshl_add_u64 v[6:7], v[6:7], 0, s[28:29]
	s_mov_b32 s6, m0
	s_mov_b32 m0, s33
	s_nop 0
	global_load_lds_dwordx4 v[6:7], off
	s_mov_b32 m0, s6
	v_lshl_add_u64 v[6:7], v[118:119], 0, s[88:89]
	s_add_i32 s6, s33, 0x2000
	v_lshl_add_u64 v[6:7], v[6:7], 0, s[30:31]
	s_mov_b32 s7, m0
	s_mov_b32 m0, s6
	s_nop 0
	global_load_lds_dwordx4 v[6:7], off
	s_mov_b32 m0, s7
	s_mul_i32 s6, s12, 0xc0000
	v_lshl_add_u64 v[2:3], v[116:117], 0, s[28:29]
	s_add_i32 s7, s33, 0x4000
	s_add_i32 s88, s6, 0x60000
	v_lshl_add_u64 v[4:5], v[118:119], 0, s[30:31]
	v_lshl_add_u64 v[6:7], v[2:3], 0, s[88:89]
	s_mov_b32 s8, m0
	s_mov_b32 m0, s7
	s_nop 0
	global_load_lds_dwordx4 v[6:7], off
	s_mov_b32 m0, s8
	s_add_i32 s7, s33, 0x6000
	v_lshl_add_u64 v[6:7], v[4:5], 0, s[88:89]
	s_mov_b32 s8, m0
	s_mov_b32 m0, s7
	s_nop 0
	global_load_lds_dwordx4 v[6:7], off
	s_mov_b32 m0, s8
	s_add_i32 s7, s33, 0x8000
	s_or_b32 s88, s6, 0x30000
	v_lshl_add_u64 v[2:3], v[2:3], 0, s[88:89]
	s_mov_b32 s8, m0
	s_mov_b32 m0, s7
	s_nop 0
	global_load_lds_dwordx4 v[2:3], off
	s_mov_b32 m0, s8
	s_add_i32 s7, s33, 0xa000
	v_lshl_add_u64 v[2:3], v[4:5], 0, s[88:89]
	s_mov_b32 s8, m0
	s_mov_b32 m0, s7
	s_nop 0
	global_load_lds_dwordx4 v[2:3], off
	s_mov_b32 m0, s8
	s_mov_b32 s7, s89
	v_lshl_add_u64 v[2:3], v[116:117], 0, s[6:7]
	v_lshl_add_u64 v[2:3], v[2:3], 0, s[28:29]
	s_add_i32 s8, s33, 0xc000
	s_mov_b32 s9, m0
	s_mov_b32 m0, s8
	s_nop 0
	global_load_lds_dwordx4 v[2:3], off
	s_mov_b32 m0, s9
	v_lshl_add_u64 v[2:3], v[118:119], 0, s[6:7]
	v_lshl_add_u64 v[2:3], v[2:3], 0, s[30:31]
	s_add_i32 s6, s33, 0xe000
	s_mov_b32 s7, m0
	s_mov_b32 m0, s6
	s_nop 0
	global_load_lds_dwordx4 v[2:3], off
	s_mov_b32 m0, s7
	v_sub_u32_e64 v0, s82, 1 clamp
	s_mov_b32 s7, 0x30000
	v_mul_lo_u32 v0, v0, s7
	v_lshl_add_u64 v[2:3], v[116:117], 0, v[0:1]
	v_lshl_add_u64 v[2:3], v[2:3], 0, s[28:29]
	s_add_i32 s6, s33, 0x10000
	s_mov_b32 s7, m0
	s_mov_b32 m0, s6
	s_nop 0
	global_load_lds_dwordx4 v[2:3], off
	s_mov_b32 m0, s7
	v_lshl_add_u64 v[2:3], v[118:119], 0, v[0:1]
	v_lshl_add_u64 v[2:3], v[2:3], 0, s[30:31]
	s_add_i32 s6, s33, 0x12000
	s_mov_b32 s7, m0
	s_mov_b32 m0, s6
	s_nop 0
	global_load_lds_dwordx4 v[2:3], off
	s_mov_b32 m0, s7
	v_lshlrev_b32_e32 v2, 4, v8
	v_lshlrev_b32_e32 v0, 1, v8
	v_and_b32_e32 v2, 0xc0, v2
	v_and_b32_e32 v0, 32, v0
	v_lshl_or_b32 v2, v9, 8, v2
	s_ashr_i32 s6, s13, 7
	v_or3_b32 v121, v2, v0, v10
	s_lshl_b32 s7, s14, 2
	v_lshlrev_b32_e32 v0, 2, v9
	v_or_b32_e32 v2, s3, v115
	s_add_i32 s88, s7, 0
	v_sub_u32_e32 v0, v2, v0
	s_lshl_b32 s7, s6, 6
	v_mov_b32_e32 v14, v1
	v_mov_b32_e32 v15, v1
	v_lshlrev_b32_e32 v114, 3, v9
	v_lshlrev_b32_e32 v123, 10, v9
	v_subrev_u32_e32 v124, s7, v0
	v_mov_b32_e32 v0, v1
	v_mov_b32_e32 v2, v1
	v_mov_b32_e32 v3, v1
	v_mov_b32_e32 v4, v1
	v_mov_b32_e32 v5, v1
	v_mov_b32_e32 v6, v1
	v_mov_b32_e32 v7, v1
	v_mov_b32_e32 v8, v1
	v_mov_b32_e32 v9, v1
	v_mov_b32_e32 v10, v1
	v_mov_b32_e32 v11, v1
	v_mov_b32_e32 v12, v1
	v_mov_b32_e32 v13, v1
	v_mov_b64_e32 v[32:33], v[14:15]
	v_mov_b64_e32 v[30:31], v[12:13]
	v_mov_b64_e32 v[28:29], v[10:11]
	v_mov_b64_e32 v[26:27], v[8:9]
	v_mov_b64_e32 v[24:25], v[6:7]
	v_mov_b64_e32 v[22:23], v[4:5]
	v_mov_b64_e32 v[20:21], v[2:3]
	v_mov_b64_e32 v[18:19], v[0:1]
	v_mov_b64_e32 v[16:17], v[14:15]
	s_mov_b32 s2, 5
	s_add_i32 s83, s82, 4
	s_add_i32 s88, s88, 0x20200
	v_lshlrev_b32_e32 v122, 4, v115
	s_mov_b32 s81, 0
	v_cmp_eq_u32_e64 s[8:9], 0, v120
	s_add_i32 s76, s95, 4
	s_sub_i32 s97, 0, s6
	v_mov_b32_e32 v125, 1.0
	s_mov_b64 s[10:11], 0
	s_mov_b32 s80, -2
	s_mov_b32 s77, 0
	s_mov_b32 s6, 0
	v_mov_b64_e32 v[14:15], v[12:13]
	v_mov_b64_e32 v[12:13], v[10:11]
	v_mov_b64_e32 v[10:11], v[8:9]
	v_mov_b64_e32 v[8:9], v[6:7]
	v_mov_b64_e32 v[6:7], v[4:5]
	v_mov_b64_e32 v[4:5], v[2:3]
	v_mov_b64_e32 v[2:3], v[0:1]
	s_waitcnt vmcnt(0)
	s_branch .LBB0_878
